# nt on the residual-tile loads of the three EpiRes epilogues and on the Q4 row loads
# baseline (speedup 1.0000x reference)
.LBB0_713:
	s_lshl_b32 s12, s11, 8
	s_lshl_b32 s8, s10, 8
	v_add_u32_e32 v132, s12, v139
	s_ashr_i32 s9, s8, 31
	v_ashrrev_i32_e32 v133, 31, v132
	v_mov_b32_e32 v131, s9
	v_or_b32_e32 v130, s8, v128
	v_lshlrev_b64 v[134:135], 11, v[132:133]
	v_lshl_add_u64 v[134:135], v[134:135], 0, v[130:131]
	v_lshl_add_u64 v[150:151], v[134:135], 1, s[4:5]
	global_load_dwordx4 v[146:149], v[150:151], off nt
	global_load_dwordx4 v[164:167], v[150:151], off offset:256 nt
	v_add_u32_e32 v156, s12, v140
	v_ashrrev_i32_e32 v157, 31, v156
	v_lshlrev_b64 v[156:157], 11, v[156:157]
	v_lshl_add_u64 v[156:157], v[156:157], 0, v[130:131]
	v_lshl_add_u64 v[156:157], v[156:157], 1, s[4:5]
	global_load_dwordx4 v[174:177], v[156:157], off nt
	global_load_dwordx4 v[178:181], v[156:157], off offset:256 nt
	v_add_u32_e32 v156, s12, v141
	v_ashrrev_i32_e32 v157, 31, v156
	v_lshlrev_b64 v[156:157], 11, v[156:157]
	v_lshl_add_u64 v[156:157], v[156:157], 0, v[130:131]
	v_lshl_add_u64 v[156:157], v[156:157], 1, s[4:5]
	global_load_dwordx4 v[182:185], v[156:157], off nt
	global_load_dwordx4 v[198:201], v[156:157], off offset:256 nt
	v_add_u32_e32 v156, s12, v142
	v_ashrrev_i32_e32 v157, 31, v156
	v_lshlrev_b64 v[156:157], 11, v[156:157]
	v_lshl_add_u64 v[156:157], v[156:157], 0, v[130:131]
	v_lshl_add_u64 v[156:157], v[156:157], 1, s[4:5]
	global_load_dwordx4 v[202:205], v[156:157], off nt
	global_load_dwordx4 v[206:209], v[156:157], off offset:256 nt
	v_add_u32_e32 v156, 0x80, v132
	v_ashrrev_i32_e32 v157, 31, v156
	v_lshlrev_b64 v[156:157], 11, v[156:157]
	v_lshl_add_u64 v[156:157], v[156:157], 0, v[130:131]
	v_lshl_add_u64 v[156:157], v[156:157], 1, s[4:5]
	global_load_dwordx4 v[210:213], v[156:157], off nt
	global_load_dwordx4 v[214:217], v[156:157], off offset:256 nt
	v_add_u32_e32 v156, 0x90, v132
	v_ashrrev_i32_e32 v157, 31, v156
	v_lshlrev_b64 v[156:157], 11, v[156:157]
	v_lshl_add_u64 v[156:157], v[156:157], 0, v[130:131]
	v_lshl_add_u64 v[156:157], v[156:157], 1, s[4:5]
	global_load_dwordx4 v[224:227], v[156:157], off nt
	global_load_dwordx4 v[228:231], v[156:157], off offset:256 nt
	v_add_u32_e32 v156, 0xa0, v132
	v_ashrrev_i32_e32 v157, 31, v156
	v_lshlrev_b64 v[156:157], 11, v[156:157]
	v_lshl_add_u64 v[156:157], v[156:157], 0, v[130:131]
	v_lshl_add_u64 v[156:157], v[156:157], 1, s[4:5]
	global_load_dwordx4 v[232:235], v[156:157], off nt
	global_load_dwordx4 v[236:239], v[156:157], off offset:256 nt
	v_add_u32_e32 v156, 0xb0, v132
	v_ashrrev_i32_e32 v157, 31, v156
	v_lshlrev_b64 v[156:157], 11, v[156:157]
	v_lshl_add_u64 v[156:157], v[156:157], 0, v[130:131]
	v_lshl_add_u64 v[156:157], v[156:157], 1, s[4:5]
	global_load_dwordx4 v[240:243], v[156:157], off nt
	global_load_dwordx4 v[244:247], v[156:157], off offset:256 nt
	v_mov_b32_e32 v161, v160
	v_cndmask_b32_e64 v145, 0, 1, s[16:17]
	v_cmp_ne_u32_e64 s[42:43], 1, v145
	s_andn2_b64 vcc, exec, s[16:17]
	s_mov_b64 s[74:75], s[96:97]
	s_waitcnt vmcnt(15)
	v_lshlrev_b32_e32 v152, 16, v146
	v_and_b32_e32 v153, 0xffff0000, v146
	v_lshlrev_b32_e32 v146, 16, v147
	v_and_b32_e32 v147, 0xffff0000, v147
	v_lshlrev_b32_e32 v154, 16, v148
	v_and_b32_e32 v155, 0xffff0000, v148
	v_lshlrev_b32_e32 v148, 16, v149
	v_and_b32_e32 v149, 0xffff0000, v149
	v_pk_fma_f32 v[126:127], v[160:161], v[126:127], v[146:147]
	v_pk_fma_f32 v[124:125], v[162:163], v[124:125], v[152:153]
	v_pk_fma_f32 v[122:123], v[160:161], v[122:123], v[148:149]
	v_pk_fma_f32 v[120:121], v[162:163], v[120:121], v[154:155]
	v_cvt_pk_bf16_f32 v146, v124, v125
	v_cvt_pk_bf16_f32 v147, v126, v127
	s_nop 0
	v_cvt_pk_bf16_f32 v148, v120, v121
	v_cvt_pk_bf16_f32 v149, v122, v123
	global_store_dwordx4 v[150:151], v[146:149], off
	s_cbranch_vccnz .LBB0_715
	s_nop 0
	v_mov_b32_e32 v146, v173
	v_mov_b32_e32 v147, v173
	v_cvt_pk_fp8_f32 v146, v124, v125
	v_cvt_pk_fp8_f32 v147, v120, v121
	v_readlane_b32 s8, v252, 21
	v_readlane_b32 s9, v252, 22
	v_cvt_pk_fp8_f32 v146, v126, v127 op_sel:[0,0,1]
	v_cvt_pk_fp8_f32 v147, v122, v123 op_sel:[0,0,1]
	v_lshl_add_u64 v[148:149], s[8:9], 0, v[134:135]
	global_store_dwordx2 v[148:149], v[146:147], off

.LBB0_785:
	s_nop 15
	s_nop 7
	s_lshl_b32 s12, s11, 8
	s_lshl_b32 s8, s10, 8
	v_add_u32_e32 v2, s12, v182
	s_ashr_i32 s9, s8, 31
	v_ashrrev_i32_e32 v3, 31, v2
	v_mov_b32_e32 v1, s9
	v_or_b32_e32 v0, s8, v164
	v_lshlrev_b64 v[4:5], 11, v[2:3]
	v_lshl_add_u64 v[4:5], v[4:5], 0, v[0:1]
	v_lshl_add_u64 v[18:19], v[4:5], 1, s[4:5]
	global_load_dwordx4 v[6:9], v[18:19], off nt
	global_load_dwordx4 v[174:177], v[18:19], off offset:256 nt
	v_add_u32_e32 v244, s12, v183
	v_ashrrev_i32_e32 v245, 31, v244
	v_lshlrev_b64 v[244:245], 11, v[244:245]
	v_lshl_add_u64 v[244:245], v[244:245], 0, v[0:1]
	v_lshl_add_u64 v[244:245], v[244:245], 1, s[4:5]
	global_load_dwordx4 v[178:181], v[244:245], off nt
	global_load_dwordx4 v[200:203], v[244:245], off offset:256 nt
	v_add_u32_e32 v244, s12, v184
	v_ashrrev_i32_e32 v245, 31, v244
	v_lshlrev_b64 v[244:245], 11, v[244:245]
	v_lshl_add_u64 v[244:245], v[244:245], 0, v[0:1]
	v_lshl_add_u64 v[244:245], v[244:245], 1, s[4:5]
	global_load_dwordx4 v[204:207], v[244:245], off nt
	global_load_dwordx4 v[208:211], v[244:245], off offset:256 nt
	v_add_u32_e32 v244, s12, v185
	v_ashrrev_i32_e32 v245, 31, v244
	v_lshlrev_b64 v[244:245], 11, v[244:245]
	v_lshl_add_u64 v[244:245], v[244:245], 0, v[0:1]
	v_lshl_add_u64 v[244:245], v[244:245], 1, s[4:5]
	global_load_dwordx4 v[212:215], v[244:245], off nt
	global_load_dwordx4 v[224:227], v[244:245], off offset:256 nt
	v_add_u32_e32 v244, 0x80, v2
	v_ashrrev_i32_e32 v245, 31, v244
	v_lshlrev_b64 v[244:245], 11, v[244:245]
	v_lshl_add_u64 v[244:245], v[244:245], 0, v[0:1]
	v_lshl_add_u64 v[244:245], v[244:245], 1, s[4:5]
	global_load_dwordx4 v[228:231], v[244:245], off nt
	global_load_dwordx4 v[236:239], v[244:245], off offset:256 nt
	v_add_u32_e32 v244, 0x90, v2
	v_ashrrev_i32_e32 v245, 31, v244
	v_lshlrev_b64 v[244:245], 11, v[244:245]
	v_lshl_add_u64 v[244:245], v[244:245], 0, v[0:1]
	v_lshl_add_u64 v[244:245], v[244:245], 1, s[4:5]
	global_load_dwordx4 v[240:243], v[244:245], off nt
	v_mov_b32_e32 v161, v160
	v_cndmask_b32_e64 v10, 0, 1, s[16:17]
	v_cmp_ne_u32_e64 s[42:43], 1, v10
	s_andn2_b64 vcc, exec, s[16:17]
	s_mov_b64 s[74:75], s[96:97]
	s_waitcnt vmcnt(10)
	v_lshlrev_b32_e32 v12, 16, v6
	v_and_b32_e32 v13, 0xffff0000, v6
	v_lshlrev_b32_e32 v6, 16, v7
	v_and_b32_e32 v7, 0xffff0000, v7
	v_lshlrev_b32_e32 v14, 16, v8
	v_and_b32_e32 v15, 0xffff0000, v8
	v_lshlrev_b32_e32 v8, 16, v9
	v_and_b32_e32 v9, 0xffff0000, v9
	v_pk_fma_f32 v[10:11], v[160:161], v[158:159], v[6:7]
	v_pk_fma_f32 v[12:13], v[162:163], v[156:157], v[12:13]
	v_pk_fma_f32 v[6:7], v[160:161], v[154:155], v[8:9]
	v_pk_fma_f32 v[8:9], v[162:163], v[152:153], v[14:15]
	v_cvt_pk_bf16_f32 v14, v12, v13
	v_cvt_pk_bf16_f32 v15, v10, v11
	s_nop 0
	v_cvt_pk_bf16_f32 v16, v8, v9
	v_cvt_pk_bf16_f32 v17, v6, v7
	global_store_dwordx4 v[18:19], v[14:17], off
	s_cbranch_vccnz .LBB0_787
	s_nop 0
	v_mov_b32_e32 v14, v173
	v_mov_b32_e32 v15, v173
	v_cvt_pk_fp8_f32 v14, v12, v13
	v_cvt_pk_fp8_f32 v15, v8, v9
	v_readlane_b32 s8, v252, 21
	v_readlane_b32 s9, v252, 22
	v_cvt_pk_fp8_f32 v14, v10, v11 op_sel:[0,0,1]
	v_cvt_pk_fp8_f32 v15, v6, v7 op_sel:[0,0,1]
	v_lshl_add_u64 v[16:17], s[8:9], 0, v[4:5]
	global_store_dwordx2 v[16:17], v[14:15], off

.LBB0_791:
	s_or_b64 exec, exec, s[10:11]
	v_add_u32_e32 v4, s12, v183
	s_waitcnt lgkmcnt(0)
	v_ashrrev_i32_e32 v5, 31, v4
	v_lshlrev_b64 v[6:7], 11, v[4:5]
	v_lshl_add_u64 v[6:7], v[6:7], 0, v[0:1]
	v_lshl_add_u64 v[20:21], v[6:7], 1, s[4:5]
	v_add_u32_e32 v244, 0x90, v2
	v_ashrrev_i32_e32 v245, 31, v244
	v_lshlrev_b64 v[244:245], 11, v[244:245]
	v_lshl_add_u64 v[244:245], v[244:245], 0, v[0:1]
	v_lshl_add_u64 v[244:245], v[244:245], 1, s[4:5]
	global_load_dwordx4 v[144:147], v[244:245], off offset:256 nt
	v_add_u32_e32 v244, 0xa0, v2
	v_ashrrev_i32_e32 v245, 31, v244
	v_lshlrev_b64 v[244:245], 11, v[244:245]
	v_lshl_add_u64 v[244:245], v[244:245], 0, v[0:1]
	v_lshl_add_u64 v[244:245], v[244:245], 1, s[4:5]
	global_load_dwordx4 v[148:151], v[244:245], off nt
	global_load_dwordx4 v[152:155], v[244:245], off offset:256 nt
	v_add_u32_e32 v244, 0xb0, v2
	v_ashrrev_i32_e32 v245, 31, v244
	v_lshlrev_b64 v[244:245], 11, v[244:245]
	v_lshl_add_u64 v[244:245], v[244:245], 0, v[0:1]
	v_lshl_add_u64 v[244:245], v[244:245], 1, s[4:5]
	global_load_dwordx4 v[156:159], v[244:245], off nt
	v_mov_b32_e32 v161, v160
	s_and_b64 vcc, exec, s[42:43]
	s_waitcnt vmcnt(14)
	v_mov_b32_e32 v8, v178
	v_mov_b32_e32 v9, v179
	v_mov_b32_e32 v10, v180
	v_mov_b32_e32 v11, v181
	v_lshlrev_b32_e32 v12, 16, v8
	v_and_b32_e32 v13, 0xffff0000, v8
	v_lshlrev_b32_e32 v8, 16, v9
	v_and_b32_e32 v9, 0xffff0000, v9
	v_lshlrev_b32_e32 v14, 16, v10
	v_and_b32_e32 v15, 0xffff0000, v10
	v_lshlrev_b32_e32 v10, 16, v11
	v_and_b32_e32 v11, 0xffff0000, v11
	v_pk_fma_f32 v[8:9], v[160:161], v[142:143], v[8:9]
	v_pk_fma_f32 v[12:13], v[162:163], v[140:141], v[12:13]
	v_pk_fma_f32 v[10:11], v[160:161], v[138:139], v[10:11]
	v_pk_fma_f32 v[14:15], v[162:163], v[136:137], v[14:15]
	v_cvt_pk_bf16_f32 v16, v12, v13
	v_cvt_pk_bf16_f32 v17, v8, v9
	s_nop 0
	v_cvt_pk_bf16_f32 v18, v14, v15
	v_cvt_pk_bf16_f32 v19, v10, v11
	global_store_dwordx4 v[20:21], v[16:19], off
	s_cbranch_vccnz .LBB0_793
	s_nop 0
	v_mov_b32_e32 v16, v173
	v_mov_b32_e32 v17, v173
	v_cvt_pk_fp8_f32 v16, v12, v13
	v_cvt_pk_fp8_f32 v17, v14, v15
	v_readlane_b32 s10, v252, 21
	v_readlane_b32 s11, v252, 22
	v_cvt_pk_fp8_f32 v16, v8, v9 op_sel:[0,0,1]
	v_cvt_pk_fp8_f32 v17, v10, v11 op_sel:[0,0,1]
	v_lshl_add_u64 v[18:19], s[10:11], 0, v[6:7]
	global_store_dwordx2 v[18:19], v[16:17], off

.LBB0_797:
	s_or_b64 exec, exec, s[10:11]
	v_add_u32_e32 v4, s12, v184
	v_ashrrev_i32_e32 v5, 31, v4
	s_waitcnt lgkmcnt(0)
	v_lshlrev_b64 v[6:7], 11, v[4:5]
	v_lshl_add_u64 v[6:7], v[6:7], 0, v[0:1]
	v_lshl_add_u64 v[20:21], v[6:7], 1, s[4:5]
	v_add_u32_e32 v244, 0xb0, v2
	v_ashrrev_i32_e32 v245, 31, v244
	v_lshlrev_b64 v[244:245], 11, v[244:245]
	v_lshl_add_u64 v[244:245], v[244:245], 0, v[0:1]
	v_lshl_add_u64 v[244:245], v[244:245], 1, s[4:5]
	global_load_dwordx4 v[128:131], v[244:245], off offset:256 nt
	v_mov_b32_e32 v161, v160
	s_and_b64 vcc, exec, s[42:43]
	s_waitcnt vmcnt(15)
	v_mov_b32_e32 v8, v204
	v_mov_b32_e32 v9, v205
	v_mov_b32_e32 v10, v206
	v_mov_b32_e32 v11, v207
	v_lshlrev_b32_e32 v12, 16, v8
	v_and_b32_e32 v13, 0xffff0000, v8
	v_lshlrev_b32_e32 v8, 16, v9
	v_and_b32_e32 v9, 0xffff0000, v9
	v_lshlrev_b32_e32 v14, 16, v10
	v_and_b32_e32 v15, 0xffff0000, v10
	v_lshlrev_b32_e32 v10, 16, v11
	v_and_b32_e32 v11, 0xffff0000, v11
	v_pk_fma_f32 v[8:9], v[160:161], v[126:127], v[8:9]
	v_pk_fma_f32 v[12:13], v[162:163], v[124:125], v[12:13]
	v_pk_fma_f32 v[10:11], v[160:161], v[122:123], v[10:11]
	v_pk_fma_f32 v[14:15], v[162:163], v[120:121], v[14:15]
	v_cvt_pk_bf16_f32 v16, v12, v13
	v_cvt_pk_bf16_f32 v17, v8, v9
	s_nop 0
	v_cvt_pk_bf16_f32 v18, v14, v15
	v_cvt_pk_bf16_f32 v19, v10, v11
	global_store_dwordx4 v[20:21], v[16:19], off
	s_cbranch_vccnz .LBB0_799
	s_nop 0
	v_mov_b32_e32 v16, v173
	v_mov_b32_e32 v17, v173
	v_cvt_pk_fp8_f32 v16, v12, v13
	v_cvt_pk_fp8_f32 v17, v14, v15
	v_readlane_b32 s10, v252, 21
	v_readlane_b32 s11, v252, 22
	v_cvt_pk_fp8_f32 v16, v8, v9 op_sel:[0,0,1]
	v_cvt_pk_fp8_f32 v17, v10, v11 op_sel:[0,0,1]
	v_lshl_add_u64 v[18:19], s[10:11], 0, v[6:7]
	global_store_dwordx2 v[18:19], v[16:17], off

.LBB0_885:
	s_or_b64 exec, exec, s[0:1]
	v_readlane_b32 s0, v253, 35
	v_readlane_b32 s1, v253, 36
	s_and_b64 vcc, exec, s[0:1]
	s_waitcnt lgkmcnt(0)
	s_barrier
	s_cbranch_vccnz .LBB0_954
	s_mov_b32 s1, s60
	s_lshl_b32 s0, s55, 3
	v_mbcnt_lo_u32_b32 v0, -1, s1
	v_mbcnt_hi_u32_b32 v0, -1, v0
	v_readlane_b32 s1, v252, 23
	s_nop 1
	v_add_u32_e32 v0, s1, v0
	s_nop 0
	v_readfirstlane_b32 s1, v0
	s_ashr_i32 s1, s1, 6
	s_add_i32 s2, s1, s0
	s_cmpk_gt_i32 s2, 0x1fff
	s_cbranch_scc1 .LBB0_905
	v_and_b32_e32 v18, 63, v0
	v_cmp_gt_u32_e64 s[38:39], 32, v18
	v_cmp_lt_u32_e32 vcc, 31, v18
	s_and_saveexec_b64 s[0:1], vcc
	s_xor_b64 s[0:1], exec, s[0:1]
	s_or_saveexec_b64 s[0:1], s[0:1]
	s_ashr_i32 s3, s2, 31
	v_mov_b32_e32 v38, 0
	v_mov_b32_e32 v39, 0
	s_xor_b64 exec, exec, s[0:1]
	s_cbranch_execz .LBB0_889
	s_lshl_b64 s[8:9], s[2:3], 7
	s_add_u32 s8, s50, s8
	s_addc_u32 s9, s51, s9
	v_lshlrev_b32_e32 v0, 2, v18
	global_load_dword v39, v0, s[8:9] nt
.LBB0_889:
	s_or_b64 exec, exec, s[0:1]
	v_readlane_b32 s8, v253, 9
	s_lshl_b32 s12, s8, 3
	s_lshl_b64 s[0:1], s[2:3], 12
	s_add_u32 s0, s4, s0
	s_addc_u32 s1, s5, s1
	v_lshlrev_b32_e32 v172, 3, v18
	global_load_dwordx2 v[0:1], v172, s[0:1] nt
	global_load_dwordx2 v[2:3], v172, s[0:1] offset:512 nt
	global_load_dwordx2 v[4:5], v172, s[0:1] offset:1024 nt
	global_load_dwordx2 v[6:7], v172, s[0:1] offset:1536 nt
	global_load_dwordx2 v[8:9], v172, s[0:1] offset:2048 nt
	global_load_dwordx2 v[10:11], v172, s[0:1] offset:2560 nt
	global_load_dwordx2 v[12:13], v172, s[0:1] offset:3072 nt
	global_load_dwordx2 v[14:15], v172, s[0:1] offset:3584 nt
	v_and_b32_e32 v16, 64, v188
	v_add_u32_e32 v16, 64, v16
	v_xor_b32_e32 v17, 1, v188
	v_cmp_lt_i32_e32 vcc, v17, v16
	v_readlane_b32 s0, v252, 21
	v_lshlrev_b32_e32 v20, 2, v18
	v_cndmask_b32_e32 v17, v188, v17, vcc
	v_lshlrev_b32_e32 v40, 2, v17
	v_xor_b32_e32 v17, 2, v188
	v_cmp_lt_i32_e32 vcc, v17, v16
	v_mov_b32_e32 v21, v173
	v_readlane_b32 s1, v252, 22
	v_cndmask_b32_e32 v17, v188, v17, vcc
	v_lshlrev_b32_e32 v41, 2, v17
	v_xor_b32_e32 v17, 4, v188
	v_cmp_lt_i32_e32 vcc, v17, v16
	v_cmp_eq_u32_e64 s[40:41], 0, v18
	v_lshl_add_u64 v[18:19], s[50:51], 0, v[20:21]
	v_cndmask_b32_e32 v17, v188, v17, vcc
	v_lshlrev_b32_e32 v42, 2, v17
	v_xor_b32_e32 v17, 8, v188
	v_cmp_lt_i32_e32 vcc, v17, v16
	s_lshl_b32 s13, s8, 4
	v_mov_b32_e32 v22, 0
	v_cndmask_b32_e32 v17, v188, v17, vcc
	v_lshlrev_b32_e32 v43, 2, v17
	v_xor_b32_e32 v17, 16, v188
	v_cmp_lt_i32_e32 vcc, v17, v16
	v_mov_b32_e32 v23, v38
	v_mov_b32_e32 v24, 0
	v_cndmask_b32_e32 v17, v188, v17, vcc
	v_lshlrev_b32_e32 v44, 2, v17
	v_xor_b32_e32 v17, 32, v188
	v_cmp_lt_i32_e32 vcc, v17, v16
	v_mov_b32_e32 v25, v38
	v_mov_b32_e32 v26, 0
	v_cndmask_b32_e32 v16, v188, v17, vcc
	v_lshlrev_b32_e32 v45, 2, v16
	v_lshl_add_u64 v[16:17], s[0:1], 0, v[20:21]
	v_lshl_add_u64 v[20:21], s[4:5], 0, v[172:173]
	v_mov_b32_e32 v27, v38
	v_mov_b32_e32 v28, 0
	v_mov_b32_e32 v29, v38
	v_mov_b32_e32 v30, 0
	v_mov_b32_e32 v31, v38
	v_mov_b32_e32 v32, 0
	v_mov_b32_e32 v33, v38
	v_mov_b32_e32 v34, 0
	v_mov_b32_e32 v35, v38
	v_mov_b32_e32 v36, 0
	v_mov_b32_e32 v37, v38
	s_branch .LBB0_892

.LBB0_892:
	s_add_i32 s0, s2, s12
	s_cmpk_lt_i32 s0, 0x2000
	s_cselect_b64 s[8:9], -1, 0
	s_cmpk_gt_i32 s0, 0x1fff
	s_cbranch_scc1 .LBB0_896
	s_ashr_i32 s1, s0, 31
	v_mov_b32_e32 v38, 0
	s_and_saveexec_b64 s[10:11], s[38:39]
	s_cbranch_execz .LBB0_895
	s_lshl_b64 s[14:15], s[0:1], 7
	v_lshl_add_u64 v[22:23], v[18:19], 0, s[14:15]
	global_load_dword v38, v[22:23], off nt
.LBB0_895:
	s_or_b64 exec, exec, s[10:11]
	s_lshl_b64 s[10:11], s[0:1], 12
	v_lshl_add_u64 v[36:37], v[20:21], 0, s[10:11]
	global_load_dwordx2 v[22:23], v[36:37], off nt
	global_load_dwordx2 v[24:25], v[36:37], off offset:512 nt
	global_load_dwordx2 v[26:27], v[36:37], off offset:1024 nt
	global_load_dwordx2 v[28:29], v[36:37], off offset:1536 nt
	global_load_dwordx2 v[30:31], v[36:37], off offset:2048 nt
	global_load_dwordx2 v[32:33], v[36:37], off offset:2560 nt
	global_load_dwordx2 v[34:35], v[36:37], off offset:3072 nt
	s_nop 0
	global_load_dwordx2 v[36:37], v[36:37], off offset:3584 nt

.LBB0_898:
	s_or_b64 exec, exec, s[10:11]
	s_mov_b64 s[10:11], -1
	s_andn2_b64 vcc, exec, s[8:9]
	v_readfirstlane_b32 s1, v0
	s_cbranch_vccnz .LBB0_891
	s_add_i32 s2, s13, s2
	s_cmpk_gt_i32 s2, 0x1fff
	s_cbranch_scc1 .LBB0_903
	s_ashr_i32 s3, s2, 31
	v_mov_b32_e32 v39, 0
	s_and_saveexec_b64 s[8:9], s[38:39]
	s_cbranch_execz .LBB0_902
	s_lshl_b64 s[10:11], s[2:3], 7
	v_lshl_add_u64 v[0:1], v[18:19], 0, s[10:11]
	global_load_dword v39, v[0:1], off nt
.LBB0_902:
	s_or_b64 exec, exec, s[8:9]
	s_lshl_b64 s[2:3], s[2:3], 12
	v_lshl_add_u64 v[14:15], v[20:21], 0, s[2:3]
	global_load_dwordx2 v[0:1], v[14:15], off nt
	global_load_dwordx2 v[2:3], v[14:15], off offset:512 nt
	global_load_dwordx2 v[4:5], v[14:15], off offset:1024 nt
	global_load_dwordx2 v[6:7], v[14:15], off offset:1536 nt
	global_load_dwordx2 v[8:9], v[14:15], off offset:2048 nt
	global_load_dwordx2 v[10:11], v[14:15], off offset:2560 nt
	global_load_dwordx2 v[12:13], v[14:15], off offset:3072 nt
	s_nop 0
	global_load_dwordx2 v[14:15], v[14:15], off offset:3584 nt

.LBB0_1161:
	s_nop 15
	s_nop 7
	s_lshl_b32 s12, s10, 8
	v_add_u32_e32 v2, s12, v165
	s_lshl_b32 s8, s11, 8
	v_ashrrev_i32_e32 v3, 31, v2
	s_ashr_i32 s9, s8, 31
	v_lshlrev_b64 v[4:5], 12, v[2:3]
	v_mov_b32_e32 v1, s9
	v_or_b32_e32 v0, s8, v164
	v_lshl_add_u64 v[4:5], s[4:5], 0, v[4:5]
	v_lshl_add_u64 v[8:9], v[0:1], 1, v[4:5]
	global_load_dwordx4 v[4:7], v[8:9], off nt
	global_load_dwordx4 v[28:31], v[8:9], off offset:256 nt
	v_add_u32_e32 v26, s12, v166
	v_ashrrev_i32_e32 v27, 31, v26
	v_lshlrev_b64 v[26:27], 12, v[26:27]
	v_lshl_add_u64 v[26:27], s[4:5], 0, v[26:27]
	v_lshl_add_u64 v[26:27], v[0:1], 1, v[26:27]
	global_load_dwordx4 v[174:177], v[26:27], off nt
	global_load_dwordx4 v[178:181], v[26:27], off offset:256 nt
	v_add_u32_e32 v26, s12, v167
	v_ashrrev_i32_e32 v27, 31, v26
	v_lshlrev_b64 v[26:27], 12, v[26:27]
	v_lshl_add_u64 v[26:27], s[4:5], 0, v[26:27]
	v_lshl_add_u64 v[26:27], v[0:1], 1, v[26:27]
	global_load_dwordx4 v[198:201], v[26:27], off nt
	global_load_dwordx4 v[202:205], v[26:27], off offset:256 nt
	v_add_u32_e32 v26, s12, v172
	v_ashrrev_i32_e32 v27, 31, v26
	v_lshlrev_b64 v[26:27], 12, v[26:27]
	v_lshl_add_u64 v[26:27], s[4:5], 0, v[26:27]
	v_lshl_add_u64 v[26:27], v[0:1], 1, v[26:27]
	global_load_dwordx4 v[206:209], v[26:27], off nt
	global_load_dwordx4 v[210:213], v[26:27], off offset:256 nt
	v_add_u32_e32 v26, 0x80, v2
	v_ashrrev_i32_e32 v27, 31, v26
	v_lshlrev_b64 v[26:27], 12, v[26:27]
	v_lshl_add_u64 v[26:27], s[4:5], 0, v[26:27]
	v_lshl_add_u64 v[26:27], v[0:1], 1, v[26:27]
	global_load_dwordx4 v[224:227], v[26:27], off nt
	global_load_dwordx4 v[228:231], v[26:27], off offset:256 nt
	v_add_u32_e32 v26, 0x90, v2
	v_ashrrev_i32_e32 v27, 31, v26
	v_lshlrev_b64 v[26:27], 12, v[26:27]
	v_lshl_add_u64 v[26:27], s[4:5], 0, v[26:27]
	v_lshl_add_u64 v[26:27], v[0:1], 1, v[26:27]
	global_load_dwordx4 v[236:239], v[26:27], off nt
	global_load_dwordx4 v[240:243], v[26:27], off offset:256 nt
	v_add_u32_e32 v26, 0xa0, v2
	v_ashrrev_i32_e32 v27, 31, v26
	v_lshlrev_b64 v[26:27], 12, v[26:27]
	v_lshl_add_u64 v[26:27], s[4:5], 0, v[26:27]
	v_lshl_add_u64 v[26:27], v[0:1], 1, v[26:27]
	global_load_dwordx4 v[244:247], v[26:27], off nt
	s_mov_b32 s10, 0x3d000000
	s_lshl_b32 s8, s11, 2
	s_ashr_i32 s9, s8, 31
	s_waitcnt vmcnt(12)
	v_lshlrev_b32_e32 v10, 16, v4
	v_and_b32_e32 v11, 0xffff0000, v4
	v_lshlrev_b32_e32 v4, 16, v5
	v_and_b32_e32 v5, 0xffff0000, v5
	v_lshlrev_b32_e32 v12, 16, v6
	v_and_b32_e32 v13, 0xffff0000, v6
	v_lshlrev_b32_e32 v6, 16, v7
	v_and_b32_e32 v7, 0xffff0000, v7
	v_pk_fma_f32 v[14:15], v[158:159], s[10:11], v[4:5] op_sel_hi:[1,0,1]
	v_pk_fma_f32 v[10:11], v[156:157], s[10:11], v[10:11] op_sel_hi:[1,0,1]
	v_pk_fma_f32 v[16:17], v[154:155], s[10:11], v[6:7] op_sel_hi:[1,0,1]
	v_cvt_pk_bf16_f32 v4, v10, v11
	v_cvt_pk_bf16_f32 v5, v14, v15
	v_pk_fma_f32 v[12:13], v[152:153], s[10:11], v[12:13] op_sel_hi:[1,0,1]
	s_nop 0
	v_cvt_pk_bf16_f32 v6, v12, v13
	v_cvt_pk_bf16_f32 v7, v16, v17
	global_store_dwordx4 v[8:9], v[4:7], off
	s_nop 1
	v_mul_f32_e32 v4, v11, v11
	v_mul_f32_e32 v5, v15, v15
	v_fmac_f32_e32 v4, v10, v10
	v_fmac_f32_e32 v5, v14, v14
	v_add_f32_e32 v4, v4, v5
	v_mul_f32_e32 v5, v13, v13
	v_fmac_f32_e32 v5, v12, v12
	v_add_f32_e32 v4, v5, v4
	v_mul_f32_e32 v5, v17, v17
	v_fmac_f32_e32 v5, v16, v16
	v_add_f32_e32 v18, v5, v4
	s_nop 0
	s_waitcnt vmcnt(12)
	v_mov_b32_e32 v4, v28
	v_mov_b32_e32 v5, v29
	v_mov_b32_e32 v6, v30
	v_mov_b32_e32 v7, v31
	v_lshlrev_b32_e32 v10, 16, v4
	v_and_b32_e32 v11, 0xffff0000, v4
	v_lshlrev_b32_e32 v4, 16, v5
	v_and_b32_e32 v5, 0xffff0000, v5
	v_lshlrev_b32_e32 v12, 16, v6
	v_and_b32_e32 v13, 0xffff0000, v6
	v_lshlrev_b32_e32 v6, 16, v7
	v_and_b32_e32 v7, 0xffff0000, v7
	v_pk_fma_f32 v[14:15], v[150:151], s[10:11], v[4:5] op_sel_hi:[1,0,1]
	v_pk_fma_f32 v[10:11], v[148:149], s[10:11], v[10:11] op_sel_hi:[1,0,1]
	v_pk_fma_f32 v[16:17], v[146:147], s[10:11], v[6:7] op_sel_hi:[1,0,1]
	v_cvt_pk_bf16_f32 v4, v10, v11
	v_cvt_pk_bf16_f32 v5, v14, v15
	v_pk_fma_f32 v[12:13], v[144:145], s[10:11], v[12:13] op_sel_hi:[1,0,1]
	s_nop 0
	v_cvt_pk_bf16_f32 v6, v12, v13
	v_cvt_pk_bf16_f32 v7, v16, v17
	global_store_dwordx4 v[8:9], v[4:7], off offset:256
	s_nop 1
	v_mul_f32_e32 v4, v11, v11
	v_mul_f32_e32 v5, v15, v15
	v_fmac_f32_e32 v4, v10, v10
	v_fmac_f32_e32 v5, v14, v14
	v_add_f32_e32 v4, v4, v5
	v_mul_f32_e32 v5, v13, v13
	v_fmac_f32_e32 v5, v12, v12
	v_add_f32_e32 v4, v5, v4
	v_mul_f32_e32 v5, v17, v17
	v_fmac_f32_e32 v5, v16, v16
	v_and_b32_e32 v6, 64, v188
	v_add_f32_e32 v4, v5, v4
	v_xor_b32_e32 v5, 16, v188
	v_add_u32_e32 v7, 64, v6
	v_cmp_lt_i32_e32 vcc, v5, v7
	v_add_f32_e32 v4, v18, v4
	s_nop 0
	v_cndmask_b32_e32 v5, v188, v5, vcc
	v_lshlrev_b32_e32 v6, 2, v5
	ds_bpermute_b32 v5, v6, v4
	s_waitcnt lgkmcnt(0)
	v_add_f32_e32 v4, v4, v5
	v_xor_b32_e32 v5, 32, v188
	v_cmp_lt_i32_e32 vcc, v5, v7
	s_nop 1
	v_cndmask_b32_e32 v5, v188, v5, vcc
	v_lshlrev_b32_e32 v7, 2, v5
	ds_bpermute_b32 v5, v7, v4
	s_and_saveexec_b64 s[10:11], s[38:39]
	s_mov_b64 s[74:75], s[96:97]
	s_cbranch_execz .LBB0_1163
	v_lshlrev_b64 v[8:9], 7, v[2:3]
	v_lshl_add_u64 v[8:9], s[50:51], 0, v[8:9]
	v_lshl_add_u64 v[8:9], s[8:9], 2, v[8:9]
	s_lshl_b32 s14, s17, 2
	s_mov_b32 s15, s60
	v_lshl_add_u64 v[8:9], v[8:9], 0, s[14:15]
	s_waitcnt lgkmcnt(0)
	v_add_f32_e32 v3, v4, v5
	global_store_dword v[8:9], v3, off
.LBB0_1163:
	s_or_b64 exec, exec, s[10:11]
	v_add_u32_e32 v4, s12, v166
	s_waitcnt lgkmcnt(0)
	v_ashrrev_i32_e32 v5, 31, v4
	v_lshlrev_b64 v[8:9], 12, v[4:5]
	v_lshl_add_u64 v[8:9], s[4:5], 0, v[8:9]
	v_lshl_add_u64 v[16:17], v[0:1], 1, v[8:9]
	v_add_u32_e32 v26, 0xa0, v2
	v_ashrrev_i32_e32 v27, 31, v26
	v_lshlrev_b64 v[26:27], 12, v[26:27]
	v_lshl_add_u64 v[26:27], s[4:5], 0, v[26:27]
	v_lshl_add_u64 v[26:27], v[0:1], 1, v[26:27]
	global_load_dwordx4 v[144:147], v[26:27], off offset:256 nt
	v_add_u32_e32 v26, 0xb0, v2
	v_ashrrev_i32_e32 v27, 31, v26
	v_lshlrev_b64 v[26:27], 12, v[26:27]
	v_lshl_add_u64 v[26:27], s[4:5], 0, v[26:27]
	v_lshl_add_u64 v[26:27], v[0:1], 1, v[26:27]
	global_load_dwordx4 v[148:151], v[26:27], off nt
	global_load_dwordx4 v[152:155], v[26:27], off offset:256 nt
	s_mov_b32 s10, 0x3d000000
	s_waitcnt vmcnt(15)
	v_mov_b32_e32 v8, v174
	v_mov_b32_e32 v9, v175
	v_mov_b32_e32 v10, v176
	v_mov_b32_e32 v11, v177
	v_lshlrev_b32_e32 v12, 16, v8
	v_and_b32_e32 v13, 0xffff0000, v8
	v_lshlrev_b32_e32 v8, 16, v9
	v_and_b32_e32 v9, 0xffff0000, v9
	v_lshlrev_b32_e32 v14, 16, v10
	v_and_b32_e32 v15, 0xffff0000, v10
	v_lshlrev_b32_e32 v10, 16, v11
	v_and_b32_e32 v11, 0xffff0000, v11
	v_pk_fma_f32 v[18:19], v[142:143], s[10:11], v[8:9] op_sel_hi:[1,0,1]
	v_pk_fma_f32 v[20:21], v[140:141], s[10:11], v[12:13] op_sel_hi:[1,0,1]
	v_pk_fma_f32 v[22:23], v[138:139], s[10:11], v[10:11] op_sel_hi:[1,0,1]
	v_pk_fma_f32 v[24:25], v[136:137], s[10:11], v[14:15] op_sel_hi:[1,0,1]
	v_cvt_pk_bf16_f32 v8, v20, v21
	v_cvt_pk_bf16_f32 v9, v18, v19
	v_mul_f32_e32 v3, v21, v21
	v_cvt_pk_bf16_f32 v10, v24, v25
	v_cvt_pk_bf16_f32 v11, v22, v23
	s_nop 0
	v_mul_f32_e32 v19, v19, v19
	v_mul_f32_e32 v21, v25, v25
	v_fmac_f32_e32 v3, v20, v20
	v_fmac_f32_e32 v19, v18, v18
	v_mul_f32_e32 v23, v23, v23
	v_fmac_f32_e32 v21, v24, v24
	v_add_f32_e32 v3, v3, v19
	v_fmac_f32_e32 v23, v22, v22
	v_add_f32_e32 v3, v21, v3
	v_add_f32_e32 v3, v23, v3
	global_store_dwordx4 v[16:17], v[8:11], off
	s_waitcnt vmcnt(15)
	v_mov_b32_e32 v12, v178
	v_mov_b32_e32 v13, v179
	v_mov_b32_e32 v14, v180
	v_mov_b32_e32 v15, v181
	v_lshlrev_b32_e32 v18, 16, v12
	v_and_b32_e32 v19, 0xffff0000, v12
	v_lshlrev_b32_e32 v12, 16, v13
	v_and_b32_e32 v13, 0xffff0000, v13
	v_lshlrev_b32_e32 v20, 16, v14
	v_and_b32_e32 v21, 0xffff0000, v14
	v_pk_fma_f32 v[12:13], v[134:135], s[10:11], v[12:13] op_sel_hi:[1,0,1]
	v_pk_fma_f32 v[18:19], v[132:133], s[10:11], v[18:19] op_sel_hi:[1,0,1]
	v_lshlrev_b32_e32 v14, 16, v15
	v_and_b32_e32 v15, 0xffff0000, v15
	v_pk_fma_f32 v[20:21], v[128:129], s[10:11], v[20:21] op_sel_hi:[1,0,1]
	v_mul_f32_e32 v22, v19, v19
	v_mul_f32_e32 v23, v13, v13
	v_pk_fma_f32 v[14:15], v[130:131], s[10:11], v[14:15] op_sel_hi:[1,0,1]
	v_mul_f32_e32 v24, v21, v21
	v_fmac_f32_e32 v22, v18, v18
	v_fmac_f32_e32 v23, v12, v12
	v_mul_f32_e32 v25, v15, v15
	v_fmac_f32_e32 v24, v20, v20
	v_add_f32_e32 v22, v22, v23
	v_add_f32_e32 v22, v24, v22
	v_fmac_f32_e32 v25, v14, v14
	v_add_f32_e32 v22, v25, v22
	v_add_f32_e32 v3, v3, v22
	ds_bpermute_b32 v22, v6, v3
	v_cvt_pk_bf16_f32 v10, v18, v19
	v_cvt_pk_bf16_f32 v11, v12, v13
	v_cvt_pk_bf16_f32 v12, v20, v21
	v_cvt_pk_bf16_f32 v13, v14, v15
	s_waitcnt lgkmcnt(0)
	v_add_f32_e32 v3, v3, v22
	ds_bpermute_b32 v8, v7, v3
	global_store_dwordx4 v[16:17], v[10:13], off offset:256
	s_and_saveexec_b64 s[10:11], s[38:39]
	s_cbranch_execz .LBB0_1165
	v_lshlrev_b64 v[4:5], 7, v[4:5]
	v_lshl_add_u64 v[4:5], s[50:51], 0, v[4:5]
	v_lshl_add_u64 v[4:5], s[8:9], 2, v[4:5]
	s_lshl_b32 s14, s17, 2
	s_mov_b32 s15, s60
	v_lshl_add_u64 v[4:5], v[4:5], 0, s[14:15]
	s_waitcnt lgkmcnt(0)
	v_add_f32_e32 v3, v3, v8
	global_store_dword v[4:5], v3, off
